# slim worker-barrier arrive sequences (13 of 15 instances)
# speedup vs baseline: 1.0478x; 1.0061x over previous
.LBB1_8:
	s_mul_i32 s22, s2, 0x50
	s_mul_i32 s3, s2, 0xf000
	s_mul_hi_i32 s8, s22, 0x300
	s_waitcnt lgkmcnt(0)
	s_add_u32 s28, s6, s3
	s_addc_u32 s29, s7, s8
	s_lshr_b32 s68, s33, 6
	v_and_b32_e32 v106, 63, v0
	s_mov_b64 s[6:7], -1
	s_and_b64 vcc, exec, s[4:5]
	s_cbranch_vccz .LBB1_400
	s_cmpk_gt_u32 s33, 0x2ff
	s_mov_b64 s[4:5], -1
	s_cbranch_scc0 .LBB1_364
	s_load_dwordx2 s[30:31], s[0:1], 0xe0
	s_load_dwordx4 s[24:27], s[0:1], 0xd0
	s_load_dword s69, s[0:1], 0xe8
	s_ashr_i32 s23, s22, 31
	v_add_u32_e32 v6, 0xfffffd00, v0
	s_waitcnt lgkmcnt(0)
	s_barrier
	s_setprio 3
	v_mov_b32_e32 v1, 0x1ef00
	v_lshl_add_u32 v2, v6, 2, v1
	v_mov_b32_e32 v1, 0
	v_cmp_eq_u32_e64 s[20:21], 0, v106
	ds_write_b32 v2, v1
	s_waitcnt lgkmcnt(0)
	s_mov_b64 s[4:5], exec
	s_and_b64 exec, exec, s[20:21]
	v_mov_b32_e32 v1, 0x20e24
	v_mov_b32_e32 v3, 1
	ds_add_u32 v1, v3
	s_mov_b64 exec, s[4:5]
	s_load_dwordx16 s[52:67], s[0:1], 0x50
	s_load_dwordx16 s[36:51], s[0:1], 0x90
	s_setprio 0
	v_mov_b32_e32 v1, 0x20e24
	s_branch .LBB1_15

.LBB1_17:
	s_wakeup
	s_setprio 3
	s_mul_i32 s6, s2, 0x2800
	s_mul_hi_i32 s3, s2, 0x2800
	s_add_u32 s4, s54, s6
	v_mov_b32_e32 v1, 0
	s_addc_u32 s5, s55, s3
	v_lshlrev_b32_e32 v4, 2, v0
	v_mov_b32_e32 v5, v1
	s_movk_i32 s7, 0x1000
	v_lshl_add_u64 v[8:9], s[4:5], 0, v[4:5]
	v_or_b32_e32 v3, 0x1000, v4
	v_add_co_u32_e32 v28, vcc, s7, v8
	global_load_dword v26, v4, s[4:5] offset:-3072
	global_load_dword v24, v4, s[4:5] offset:-2048
	global_load_dword v22, v4, s[4:5] offset:-1024
	global_load_dword v20, v4, s[4:5]
	global_load_dword v18, v4, s[4:5] offset:1024
	global_load_dword v16, v4, s[4:5] offset:2048
	global_load_dword v12, v3, s[4:5]
	global_load_dword v14, v4, s[4:5] offset:3072
	v_addc_co_u32_e32 v29, vcc, 0, v9, vcc
	global_load_dword v10, v[28:29], off offset:1024
	s_add_u32 s4, s52, s6
	s_addc_u32 s5, s53, s3
	v_lshl_add_u64 v[32:33], s[4:5], 0, v[4:5]
	global_load_dword v31, v4, s[4:5] offset:-3072
	global_load_dword v8, v[28:29], off offset:2048
	global_load_dword v30, v4, s[4:5] offset:-2048
	global_load_dword v27, v4, s[4:5] offset:-1024
	global_load_dword v25, v4, s[4:5]
	global_load_dword v23, v4, s[4:5] offset:1024
	global_load_dword v21, v4, s[4:5] offset:2048
	global_load_dword v19, v4, s[4:5] offset:3072
	global_load_dword v17, v3, s[4:5]
	v_add_co_u32_e32 v4, vcc, s7, v32
	s_mov_b32 s3, 0x66666667
	s_nop 0
	v_addc_co_u32_e32 v5, vcc, 0, v33, vcc
	global_load_dword v15, v[4:5], off offset:1024
	global_load_dword v13, v[4:5], off offset:2048
	v_mov_b32_e32 v3, 0x1ef00
	v_mov_b32_e32 v4, 1
	s_waitcnt vmcnt(19)
	v_mul_hi_i32 v5, v26, s3
	s_waitcnt vmcnt(18)
	v_mul_hi_i32 v7, v24, s3
	v_lshrrev_b32_e32 v33, 31, v5
	v_ashrrev_i32_e32 v5, 5, v5
	s_waitcnt vmcnt(17)
	v_mul_hi_i32 v9, v22, s3
	v_lshrrev_b32_e32 v34, 31, v7
	v_ashrrev_i32_e32 v7, 5, v7
	v_add_u32_e32 v57, v5, v33
	s_waitcnt vmcnt(16)
	v_mul_hi_i32 v11, v20, s3
	s_waitcnt vmcnt(15)
	v_mul_hi_i32 v28, v18, s3
	s_waitcnt vmcnt(14)
	v_mul_hi_i32 v29, v16, s3
	s_waitcnt vmcnt(13)
	v_mul_hi_i32 v32, v12, s3
	v_lshrrev_b32_e32 v35, 31, v9
	v_ashrrev_i32_e32 v9, 5, v9
	v_add_u32_e32 v54, v7, v34
	s_waitcnt vmcnt(12)
	v_mul_hi_i32 v5, v14, s3
	v_lshl_add_u32 v60, v57, 2, v3
	v_lshrrev_b32_e32 v36, 31, v11
	v_ashrrev_i32_e32 v11, 5, v11
	v_lshrrev_b32_e32 v37, 31, v28
	v_ashrrev_i32_e32 v28, 5, v28
	v_lshrrev_b32_e32 v38, 31, v29
	v_ashrrev_i32_e32 v29, 5, v29
	v_lshrrev_b32_e32 v39, 31, v32
	v_ashrrev_i32_e32 v32, 5, v32
	v_add_u32_e32 v51, v9, v35
	s_waitcnt vmcnt(11)
	v_mul_hi_i32 v7, v10, s3
	v_lshl_add_u32 v58, v54, 2, v3
	v_lshrrev_b32_e32 v9, 31, v5
	v_ashrrev_i32_e32 v5, 5, v5
	ds_add_rtn_u32 v61, v60, v4
	v_add_u32_e32 v48, v11, v36
	v_add_u32_e32 v44, v28, v37
	v_add_u32_e32 v41, v29, v38
	v_add_u32_e32 v32, v32, v39
	v_lshl_add_u32 v55, v51, 2, v3
	v_lshrrev_b32_e32 v11, 31, v7
	v_add_u32_e32 v42, v5, v9
	ds_add_rtn_u32 v59, v58, v4
	v_ashrrev_i32_e32 v5, 5, v7
	v_lshl_add_u32 v52, v48, 2, v3
	v_lshl_add_u32 v49, v44, 2, v3
	v_lshl_add_u32 v46, v41, 2, v3
	v_lshl_add_u32 v38, v32, 2, v3
	v_lshl_add_u32 v45, v42, 2, v3
	ds_add_rtn_u32 v56, v55, v4
	ds_add_rtn_u32 v53, v52, v4
	ds_add_rtn_u32 v50, v49, v4
	ds_add_rtn_u32 v47, v46, v4
	ds_add_rtn_u32 v43, v45, v4
	ds_add_rtn_u32 v40, v38, v4
	v_add_u32_e32 v35, v5, v11
	s_waitcnt vmcnt(9)
	v_mul_hi_i32 v5, v8, s3
	v_lshrrev_b32_e32 v7, 31, v5
	v_ashrrev_i32_e32 v5, 5, v5
	v_lshl_add_u32 v39, v35, 2, v3
	v_add_u32_e32 v33, v5, v7
	ds_add_rtn_u32 v36, v39, v4
	v_lshl_add_u32 v37, v33, 2, v3
	ds_add_rtn_u32 v34, v37, v4
	s_waitcnt lgkmcnt(0)
	s_mov_b64 s[4:5], exec
	s_and_b64 exec, exec, s[20:21]
	v_mov_b32_e32 v3, 0x20e24
	v_mov_b32_e32 v4, 1
	ds_add_u32 v3, v4
	s_mov_b64 exec, s[4:5]
	s_setprio 0
	v_mov_b32_e32 v3, 0x20e24
	s_branch .LBB1_22

.LBB1_73:
	s_or_b64 exec, exec, s[4:5]
	s_waitcnt vmcnt(0)
	s_mov_b64 s[4:5], exec
	s_and_b64 exec, exec, s[20:21]
	v_mov_b32_e32 v2, 0x20e24
	v_mov_b32_e32 v3, 1
	ds_add_u32 v2, v3
	s_mov_b64 exec, s[4:5]
	s_setprio 0
	v_mov_b32_e32 v2, 0x20e24
	s_branch .LBB1_78

.LBB1_104:
	s_or_b64 exec, exec, s[6:7]
	s_waitcnt lgkmcnt(0)
	s_mov_b64 s[6:7], exec
	s_and_b64 exec, exec, s[20:21]
	v_mov_b32_e32 v2, 0x20e24
	v_mov_b32_e32 v3, 1
	ds_add_u32 v2, v3
	s_mov_b64 exec, s[6:7]
	s_setprio 0
	v_mov_b32_e32 v2, 0x20e24
	s_branch .LBB1_109

.LBB1_120:
	s_or_b64 exec, exec, s[34:35]
	s_waitcnt lgkmcnt(0)
	s_mov_b64 s[16:17], exec
	s_and_b64 exec, exec, s[20:21]
	v_mov_b32_e32 v5, 0x20e24
	v_mov_b32_e32 v65, 1
	ds_add_u32 v5, v65
	s_mov_b64 exec, s[16:17]
	s_setprio 0
	v_mov_b32_e32 v5, 0x20e24
	s_branch .LBB1_125

.LBB1_137:
	s_or_b64 exec, exec, s[16:17]
	v_sub_u32_e32 v2, v3, v2
	v_mov_b32_e32 v3, 0x1f300
	v_add_u32_e32 v2, v2, v65
	v_lshl_add_u32 v3, v6, 2, v3
	ds_write_b32 v3, v2
	s_waitcnt lgkmcnt(0)
	s_mov_b64 s[16:17], exec
	s_and_b64 exec, exec, s[20:21]
	v_mov_b32_e32 v2, 0x20e24
	v_mov_b32_e32 v3, 1
	ds_add_u32 v2, v3
	s_mov_b64 exec, s[16:17]
	s_setprio 0
	v_mov_b32_e32 v2, 0x20e24
	s_branch .LBB1_142

.LBB1_144:
	s_wakeup
	s_setprio 3
	ds_read2st64_b32 v[2:3], v60 offset0:4 offset1:8
	s_mov_b32 s3, 0xffb0
	v_mad_u64_u32 v[4:5], s[16:17], v57, s3, v[26:27]
	v_lshl_or_b32 v4, v4, 16, v31
	s_waitcnt lgkmcnt(0)
	v_add3_u32 v2, v2, v61, v3
	v_ashrrev_i32_e32 v3, 31, v2
	v_lshl_add_u64 v[2:3], v[2:3], 2, s[44:45]
	global_store_dword v[2:3], v4, off sc1
	ds_read2st64_b32 v[2:3], v58 offset0:4 offset1:8
	v_mad_u64_u32 v[4:5], s[16:17], v54, s3, v[24:25]
	v_lshl_or_b32 v4, v4, 16, v30
	s_waitcnt lgkmcnt(0)
	v_add3_u32 v2, v2, v59, v3
	v_ashrrev_i32_e32 v3, 31, v2
	v_lshl_add_u64 v[2:3], v[2:3], 2, s[44:45]
	global_store_dword v[2:3], v4, off sc1
	ds_read2st64_b32 v[2:3], v55 offset0:4 offset1:8
	v_mad_u64_u32 v[4:5], s[16:17], v51, s3, v[22:23]
	v_lshl_or_b32 v4, v4, 16, v27
	s_waitcnt lgkmcnt(0)
	v_add3_u32 v2, v2, v56, v3
	v_ashrrev_i32_e32 v3, 31, v2
	v_lshl_add_u64 v[2:3], v[2:3], 2, s[44:45]
	global_store_dword v[2:3], v4, off sc1
	ds_read2st64_b32 v[2:3], v52 offset0:4 offset1:8
	v_mad_u64_u32 v[4:5], s[16:17], v48, s3, v[20:21]
	v_lshl_or_b32 v4, v4, 16, v25
	s_waitcnt lgkmcnt(0)
	v_add3_u32 v2, v2, v53, v3
	v_ashrrev_i32_e32 v3, 31, v2
	v_lshl_add_u64 v[2:3], v[2:3], 2, s[44:45]
	global_store_dword v[2:3], v4, off sc1
	ds_read2st64_b32 v[2:3], v49 offset0:4 offset1:8
	v_mad_u64_u32 v[4:5], s[16:17], v44, s3, v[18:19]
	v_lshl_or_b32 v4, v4, 16, v23
	s_waitcnt lgkmcnt(0)
	v_add3_u32 v2, v2, v50, v3
	v_ashrrev_i32_e32 v3, 31, v2
	v_lshl_add_u64 v[2:3], v[2:3], 2, s[44:45]
	global_store_dword v[2:3], v4, off sc1
	ds_read2st64_b32 v[2:3], v46 offset0:4 offset1:8
	v_mad_u64_u32 v[4:5], s[16:17], v41, s3, v[16:17]
	v_lshl_or_b32 v4, v4, 16, v21
	s_waitcnt lgkmcnt(0)
	v_add3_u32 v2, v2, v47, v3
	v_ashrrev_i32_e32 v3, 31, v2
	v_lshl_add_u64 v[2:3], v[2:3], 2, s[44:45]
	global_store_dword v[2:3], v4, off sc1
	ds_read2st64_b32 v[2:3], v45 offset0:4 offset1:8
	v_mad_u64_u32 v[4:5], s[16:17], v42, s3, v[14:15]
	v_lshl_or_b32 v4, v4, 16, v19
	s_waitcnt lgkmcnt(0)
	v_add3_u32 v2, v2, v43, v3
	v_ashrrev_i32_e32 v3, 31, v2
	v_lshl_add_u64 v[2:3], v[2:3], 2, s[44:45]
	global_store_dword v[2:3], v4, off sc1
	ds_read2st64_b32 v[2:3], v38 offset0:4 offset1:8
	v_mad_u64_u32 v[4:5], s[16:17], v32, s3, v[12:13]
	v_lshl_or_b32 v4, v4, 16, v17
	s_waitcnt lgkmcnt(0)
	v_add3_u32 v2, v2, v40, v3
	v_ashrrev_i32_e32 v3, 31, v2
	v_lshl_add_u64 v[2:3], v[2:3], 2, s[44:45]
	global_store_dword v[2:3], v4, off sc1
	ds_read2st64_b32 v[2:3], v39 offset0:4 offset1:8
	v_mad_u64_u32 v[4:5], s[16:17], v35, s3, v[10:11]
	v_lshl_or_b32 v4, v4, 16, v15
	s_waitcnt lgkmcnt(0)
	v_add3_u32 v2, v2, v36, v3
	v_ashrrev_i32_e32 v3, 31, v2
	v_lshl_add_u64 v[2:3], v[2:3], 2, s[44:45]
	global_store_dword v[2:3], v4, off sc1
	ds_read2st64_b32 v[2:3], v37 offset0:4 offset1:8
	v_mad_u64_u32 v[4:5], s[16:17], v33, s3, v[8:9]
	v_lshl_or_b32 v4, v4, 16, v13
	s_waitcnt lgkmcnt(0)
	v_add3_u32 v2, v2, v34, v3
	v_ashrrev_i32_e32 v3, 31, v2
	v_lshl_add_u64 v[2:3], v[2:3], 2, s[44:45]
	global_store_dword v[2:3], v4, off sc1
	s_waitcnt vmcnt(0)
	s_mov_b64 s[16:17], exec
	s_and_b64 exec, exec, s[20:21]
	v_mov_b32_e32 v2, 0x20e24
	v_mov_b32_e32 v3, 1
	ds_add_u32 v2, v3
	s_mov_b64 exec, s[16:17]
	s_setprio 0
	v_mov_b32_e32 v2, 0x20e24
	s_branch .LBB1_149

.LBB1_176:
	s_or_b64 exec, exec, s[16:17]
	s_waitcnt lgkmcnt(0)
	s_mov_b64 s[16:17], exec
	s_and_b64 exec, exec, s[20:21]
	v_mov_b32_e32 v2, 0x20e24
	v_mov_b32_e32 v3, 1
	ds_add_u32 v2, v3
	s_mov_b64 exec, s[16:17]
	s_setprio 0
	v_mov_b32_e32 v2, 0x20e24
	s_branch .LBB1_181

.LBB1_212:
	s_waitcnt lgkmcnt(0)
	s_mov_b64 s[34:35], exec
	s_and_b64 exec, exec, s[20:21]
	v_mov_b32_e32 v4, 0x20e24
	v_mov_b32_e32 v5, 1
	ds_add_u32 v4, v5
	s_mov_b64 exec, s[34:35]
	s_setprio 0
	v_mov_b32_e32 v4, 0x20e24
	s_branch .LBB1_217

.LBB1_224:
	s_or_b64 exec, exec, s[34:35]
	s_waitcnt lgkmcnt(0)
	s_mov_b64 s[6:7], exec
	s_and_b64 exec, exec, s[20:21]
	v_mov_b32_e32 v4, 0x20e24
	v_mov_b32_e32 v5, 1
	ds_add_u32 v4, v5
	s_mov_b64 exec, s[6:7]
	s_setprio 0
	v_mov_b32_e32 v4, 0x20e24
	s_branch .LBB1_229

.LBB1_267:
	s_or_b64 exec, exec, s[2:3]
	s_waitcnt vmcnt(0)
	s_mov_b64 s[2:3], exec
	s_and_b64 exec, exec, s[20:21]
	v_mov_b32_e32 v2, 0x20e24
	v_mov_b32_e32 v3, 1
	ds_add_u32 v2, v3
	s_mov_b64 exec, s[2:3]
	s_setprio 0
	v_mov_b32_e32 v2, 0x20e24
	s_branch .LBB1_272

.LBB1_299:
	s_or_b64 exec, exec, s[2:3]
	s_waitcnt lgkmcnt(0)
	s_mov_b64 s[2:3], exec
	s_and_b64 exec, exec, s[20:21]
	v_mov_b32_e32 v2, 0x20e24
	v_mov_b32_e32 v3, 1
	ds_add_u32 v2, v3
	s_mov_b64 exec, s[2:3]
	s_setprio 0
	v_mov_b32_e32 v2, 0x20e24
	s_branch .LBB1_304

.LBB1_353:
	v_lshl_or_b32 v2, s4, 8, v106
	v_ashrrev_i32_e32 v3, 31, v2
	v_lshrrev_b32_e32 v1, 2, v0
	v_lshl_add_u64 v[18:19], v[2:3], 4, s[66:67]
	v_and_b32_e32 v1, 12, v1
	global_load_dwordx4 v[2:5], v[18:19], off
	global_load_dwordx4 v[6:9], v[18:19], off offset:1024
	global_load_dwordx4 v[10:13], v[18:19], off offset:2048
	global_load_dwordx4 v[14:17], v[18:19], off offset:3072
	s_lshl_b32 s2, s4, 5
	v_mov_b32_e32 v19, 0
	v_lshlrev_b32_e32 v18, 2, v1
	v_lshl_add_u64 v[18:19], s[30:31], 0, v[18:19]
	s_ashr_i32 s3, s2, 31
	v_lshl_add_u64 v[26:27], s[2:3], 2, v[18:19]
	global_load_dwordx4 v[18:21], v[26:27], off
	global_load_dwordx4 v[22:25], v[26:27], off offset:64
	s_waitcnt lgkmcnt(0)
	s_mov_b64 s[4:5], exec
	s_and_b64 exec, exec, s[20:21]
	v_mov_b32_e32 v26, 0x20e24
	v_mov_b32_e32 v27, 1
	ds_add_u32 v26, v27
	s_mov_b64 exec, s[4:5]
	s_setprio 0
	v_mov_b32_e32 v26, 0x20e24
	s_branch .LBB1_358
